# norm1 and final norm: the residual-stream row loads (read once per phase, then overwritten in place) carry the nt hint like the expert-output loads already do, leaving cache capacity to the not-yet-re
# speedup vs baseline: 1.0095x; 1.0019x over previous
; __device__ __forceinline__ float bf_lo(unsigned w) { return __uint_as_float(w << 16); }
; __device__ __forceinline__ float bf_hi(unsigned w) { return __uint_as_float(w & 0xffff0000u); }
;     __device__ __forceinline__ float* mods() const { return (float*)(ws + WS_MODS); }
;     __device__ __forceinline__ bf16_t* Y() const { return (bf16_t*)(ws + WS_Y); }
; __device__ __forceinline__ void phase_norm1(const Frame& F, const Params& P, int l, const float* xs, long long dctx, bool combine, float* xw, long long dctxw) {
;     ...
;         const float* xr = xrow_ptr(xs, dctx, row);
;         const int b = row < TL ? (row >> 13) : 8;
;         const float* md = F.mods() + (size_t)(l * 9 + b) * 6144;
;         f32x4 v[4]; float ss = 0.f;
; #pragma unroll
;         for (int j = 0; j < 4; ++j) v[j] = *(const f32x4*)(xr + F.lane * 4 + 256 * j);
;         if (combine) {
;             const float* g5 = F.mods() + (size_t)((l - 1) * 9 + b) * 6144 + 5 * 1024;
;             const bf16_t* yr = F.Y() + (size_t)row * 4 * DM;
;             float* xo = xw + (size_t)row * DM + (row >= TL ? dctxw : 0ll);
; #pragma unroll
;             for (int j = 0; j < 4; ++j) {
;                 const int col = F.lane * 4 + 256 * j;
;                 f32x4 s = (f32x4){0.f, 0.f, 0.f, 0.f};
; #pragma unroll
;                 for (int k = 0; k < 4; ++k) { const u32x2 w = __builtin_nontemporal_load((const u32x2*)(yr + (size_t)k * DM + col));     s[0] += bf_lo(w.x); s[1] += bf_hi(w.x); s[2] += bf_lo(w.y); s[3] += bf_hi(w.y); }
;                 v[j] += *(const f32x4*)(g5 + col) * s;
;                 *(f32x4*)(xo + col) = v[j];
;             }
;         }
.LBB0_171:
	s_cmp_gt_i32 s44, 0xffff
	s_cselect_b64 s[8:9], -1, 0
	s_and_b64 s[18:19], s[8:9], exec
	s_cselect_b32 s19, s43, 0
	s_cselect_b32 s18, s42, 0
	v_lshl_add_u64 v[2:3], s[52:53], 0, v[20:21]
	v_lshl_add_u64 v[2:3], s[18:19], 2, v[2:3]
	global_load_dwordx4 v[14:17], v[2:3], off nt
	global_load_dwordx4 v[10:13], v[2:3], off offset:1024 nt
	global_load_dwordx4 v[6:9], v[2:3], off offset:2048 nt
	s_nop 0
	global_load_dwordx4 v[2:5], v[2:3], off offset:3072 nt
	s_min_i32 s2, s44, 0x10000
	s_andn2_b64 vcc, exec, s[40:41]
	s_ashr_i32 s2, s2, 13
	s_cbranch_vccnz .LBB0_170
	s_mul_i32 s18, s2, 0x6000
	s_mul_hi_i32 s7, s2, 0x6000
	s_add_u32 s18, s0, s18
	s_addc_u32 s7, s1, s7
	s_add_u32 s28, s18, 0x5000
	s_addc_u32 s29, s7, 0
	v_lshl_add_u64 v[22:23], s[46:47], 0, v[146:147]
	s_mov_b32 s7, 0x1c316000
	v_add_co_u32_e32 v24, vcc, s7, v22
	s_mov_b32 s7, 0x1c317000
	s_nop 0
	v_addc_co_u32_e32 v25, vcc, 0, v23, vcc
	global_load_dwordx2 v[32:33], v[24:25], off offset:256 nt
	global_load_dwordx2 v[34:35], v[24:25], off offset:2304 nt
	v_add_co_u32_e32 v26, vcc, s7, v22
	s_and_b64 s[8:9], s[8:9], exec
	s_nop 0
	v_addc_co_u32_e32 v27, vcc, 0, v23, vcc
	global_load_dwordx2 v[22:23], v[26:27], off offset:256 nt
	global_load_dwordx2 v[36:37], v[26:27], off offset:2304 nt
	global_load_dwordx4 v[80:83], v30, s[28:29]
	global_load_dwordx2 v[84:85], v[24:25], off offset:768 nt
	global_load_dwordx2 v[86:87], v[24:25], off offset:2816 nt
	global_load_dwordx2 v[88:89], v[26:27], off offset:768 nt
	global_load_dwordx2 v[90:91], v[26:27], off offset:2816 nt
	global_load_dwordx4 v[92:95], v1, s[28:29]
	global_load_dwordx2 v[96:97], v[24:25], off offset:1280 nt
	global_load_dwordx2 v[98:99], v[24:25], off offset:3328 nt
	global_load_dwordx2 v[100:101], v[26:27], off offset:1280 nt
	global_load_dwordx2 v[102:103], v[26:27], off offset:3328 nt
	global_load_dwordx4 v[104:107], v28, s[28:29]
	global_load_dwordx2 v[108:109], v[24:25], off offset:1792 nt
	global_load_dwordx2 v[110:111], v[24:25], off offset:3840 nt
	global_load_dwordx2 v[112:113], v[26:27], off offset:1792 nt
	global_load_dwordx2 v[114:115], v[26:27], off offset:3840 nt
	global_load_dwordx4 v[116:119], v29, s[28:29]
	s_cselect_b32 s9, s61, 0
	s_cselect_b32 s8, s60, 0
	s_waitcnt vmcnt(15)
	v_lshlrev_b32_e32 v38, 16, v32
	v_and_b32_e32 v39, 0xffff0000, v32
	v_lshlrev_b32_e32 v32, 16, v33
	v_and_b32_e32 v33, 0xffff0000, v33
	v_pk_add_f32 v[38:39], v[38:39], 0 op_sel_hi:[1,0]
	v_lshlrev_b32_e32 v40, 16, v34
	v_and_b32_e32 v41, 0xffff0000, v34
	v_pk_add_f32 v[32:33], v[32:33], 0 op_sel_hi:[1,0]
	v_lshlrev_b32_e32 v34, 16, v35
	v_and_b32_e32 v35, 0xffff0000, v35
	v_pk_add_f32 v[38:39], v[38:39], v[40:41]
	v_lshlrev_b32_e32 v40, 16, v22
	v_and_b32_e32 v41, 0xffff0000, v22
	v_pk_add_f32 v[32:33], v[32:33], v[34:35]
	v_lshlrev_b32_e32 v22, 16, v23
	v_and_b32_e32 v23, 0xffff0000, v23
	v_pk_add_f32 v[22:23], v[32:33], v[22:23]
	v_lshlrev_b32_e32 v32, 16, v37
	v_and_b32_e32 v33, 0xffff0000, v37
	v_pk_add_f32 v[22:23], v[22:23], v[32:33]
	v_pk_add_f32 v[38:39], v[38:39], v[40:41]
	v_lshlrev_b32_e32 v40, 16, v36
	v_and_b32_e32 v41, 0xffff0000, v36
	v_pk_add_f32 v[38:39], v[38:39], v[40:41]
	v_pk_fma_f32 v[16:17], v[82:83], v[22:23], v[16:17]
	v_lshl_add_u64 v[22:23], s[50:51], 0, v[20:21]
	v_pk_fma_f32 v[14:15], v[80:81], v[38:39], v[14:15]
	v_lshl_add_u64 v[22:23], s[8:9], 2, v[22:23]
	global_store_dwordx4 v[22:23], v[14:17], off
	s_waitcnt vmcnt(11)
	v_lshlrev_b32_e32 v40, 16, v84
	v_and_b32_e32 v41, 0xffff0000, v84
	v_lshlrev_b32_e32 v32, 16, v85
	v_and_b32_e32 v33, 0xffff0000, v85
	v_lshlrev_b32_e32 v42, 16, v86
	v_and_b32_e32 v43, 0xffff0000, v86
	v_pk_add_f32 v[32:33], v[32:33], 0 op_sel_hi:[1,0]
	v_lshlrev_b32_e32 v34, 16, v87
	v_and_b32_e32 v35, 0xffff0000, v87
	v_pk_add_f32 v[32:33], v[32:33], v[34:35]
	v_lshlrev_b32_e32 v34, 16, v89
	v_and_b32_e32 v35, 0xffff0000, v89
	v_pk_add_f32 v[40:41], v[40:41], 0 op_sel_hi:[1,0]
	v_pk_add_f32 v[32:33], v[32:33], v[34:35]
	v_lshlrev_b32_e32 v34, 16, v91
	v_and_b32_e32 v35, 0xffff0000, v91
	v_pk_add_f32 v[40:41], v[40:41], v[42:43]
	v_lshlrev_b32_e32 v42, 16, v88
	v_and_b32_e32 v43, 0xffff0000, v88
	v_pk_add_f32 v[36:37], v[32:33], v[34:35]
	v_pk_add_f32 v[40:41], v[40:41], v[42:43]
	v_lshlrev_b32_e32 v42, 16, v90
	v_and_b32_e32 v43, 0xffff0000, v90
	v_pk_add_f32 v[40:41], v[40:41], v[42:43]
	v_pk_fma_f32 v[12:13], v[94:95], v[36:37], v[12:13]
	v_pk_fma_f32 v[10:11], v[92:93], v[40:41], v[10:11]
	global_store_dwordx4 v[22:23], v[10:13], off offset:1024
	s_waitcnt vmcnt(7)
	v_lshlrev_b32_e32 v40, 16, v96
	v_and_b32_e32 v41, 0xffff0000, v96
	v_lshlrev_b32_e32 v32, 16, v97
	v_and_b32_e32 v33, 0xffff0000, v97
	v_lshlrev_b32_e32 v42, 16, v98
	v_and_b32_e32 v43, 0xffff0000, v98
	v_pk_add_f32 v[32:33], v[32:33], 0 op_sel_hi:[1,0]
	v_lshlrev_b32_e32 v34, 16, v99
	v_and_b32_e32 v35, 0xffff0000, v99
	v_pk_add_f32 v[32:33], v[32:33], v[34:35]
	v_lshlrev_b32_e32 v34, 16, v101
	v_and_b32_e32 v35, 0xffff0000, v101
	v_pk_add_f32 v[40:41], v[40:41], 0 op_sel_hi:[1,0]
	v_pk_add_f32 v[32:33], v[32:33], v[34:35]
	v_lshlrev_b32_e32 v34, 16, v103
	v_and_b32_e32 v35, 0xffff0000, v103
	v_pk_add_f32 v[40:41], v[40:41], v[42:43]
	v_lshlrev_b32_e32 v42, 16, v100
	v_and_b32_e32 v43, 0xffff0000, v100
	v_pk_add_f32 v[36:37], v[32:33], v[34:35]
	v_pk_add_f32 v[40:41], v[40:41], v[42:43]
	v_lshlrev_b32_e32 v42, 16, v102
	v_and_b32_e32 v43, 0xffff0000, v102
	v_pk_add_f32 v[40:41], v[40:41], v[42:43]
	v_pk_fma_f32 v[8:9], v[106:107], v[36:37], v[8:9]
	v_pk_fma_f32 v[6:7], v[104:105], v[40:41], v[6:7]
	global_store_dwordx4 v[22:23], v[6:9], off offset:2048
	s_nop 0
	s_nop 0
	s_nop 0
	s_waitcnt vmcnt(3)
	v_lshlrev_b32_e32 v36, 16, v108
	v_and_b32_e32 v37, 0xffff0000, v108
	v_lshlrev_b32_e32 v32, 16, v109
	v_and_b32_e32 v33, 0xffff0000, v109
	v_pk_add_f32 v[36:37], v[36:37], 0 op_sel_hi:[1,0]
	v_lshlrev_b32_e32 v38, 16, v110
	v_and_b32_e32 v39, 0xffff0000, v110
	v_pk_add_f32 v[32:33], v[32:33], 0 op_sel_hi:[1,0]
	v_lshlrev_b32_e32 v24, 16, v111
	v_and_b32_e32 v25, 0xffff0000, v111
	v_pk_add_f32 v[36:37], v[36:37], v[38:39]
	v_lshlrev_b32_e32 v38, 16, v112
	v_and_b32_e32 v39, 0xffff0000, v112
	v_pk_add_f32 v[24:25], v[32:33], v[24:25]
	v_lshlrev_b32_e32 v32, 16, v113
	v_and_b32_e32 v33, 0xffff0000, v113
	v_pk_add_f32 v[36:37], v[36:37], v[38:39]
	v_lshlrev_b32_e32 v38, 16, v114
	v_and_b32_e32 v39, 0xffff0000, v114
	v_pk_add_f32 v[24:25], v[24:25], v[32:33]
	v_lshlrev_b32_e32 v26, 16, v115
	v_and_b32_e32 v27, 0xffff0000, v115
	v_pk_add_f32 v[32:33], v[24:25], v[26:27]
	v_pk_add_f32 v[36:37], v[36:37], v[38:39]
	v_pk_fma_f32 v[4:5], v[118:119], v[32:33], v[4:5]
	v_pk_fma_f32 v[2:3], v[116:117], v[36:37], v[2:3]
	global_store_dwordx4 v[22:23], v[2:5], off offset:3072
	s_branch .LBB0_170

; __device__ __forceinline__ float bf_lo(unsigned w) { return __uint_as_float(w << 16); }
; __device__ __forceinline__ float bf_hi(unsigned w) { return __uint_as_float(w & 0xffff0000u); }
;     __device__ __forceinline__ float* mods() const { return (float*)(ws + WS_MODS); }
;     __device__ __forceinline__ bf16_t* Y() const { return (bf16_t*)(ws + WS_Y); }
; __device__ __forceinline__ void phase_final(const Frame& F, const Params& P) {
;     ...
;         float* xr = P.out + (size_t)row * DM;
;         const float* g5 = F.mods() + (size_t)((NLAYER - 1) * 9 + (row >> 13)) * 6144 + 5 * 1024;
;         const bf16_t* yr = F.Y() + (size_t)row * 4 * DM;
;         f32x4 v[4]; float ss = 0.f;
; #pragma unroll
;         for (int j = 0; j < 4; ++j) {
;             const int col = F.lane * 4 + 256 * j;
;             v[j] = *(const f32x4*)(xr + col);
;             f32x4 s = (f32x4){0.f, 0.f, 0.f, 0.f};
; #pragma unroll
;             for (int k = 0; k < 4; ++k) { const u32x2 w = __builtin_nontemporal_load((const u32x2*)(yr + (size_t)k * DM + col));     s[0] += bf_lo(w.x); s[1] += bf_hi(w.x); s[2] += bf_lo(w.y); s[3] += bf_hi(w.y); }
;             v[j] += *(const f32x4*)(g5 + col) * s;
.LBB0_1932:
	s_ashr_i32 s3, s0, 13
	v_add_co_u32_e32 v36, vcc, s1, v0
	s_add_i32 s3, s3, 9
	global_load_dwordx2 v[8:9], v[0:1], off nt
	global_load_dwordx2 v[6:7], v[0:1], off offset:2048 nt
	global_load_dwordx2 v[52:53], v[0:1], off offset:512 nt
	global_load_dwordx2 v[54:55], v[0:1], off offset:2560 nt
	global_load_dwordx2 v[56:57], v[0:1], off offset:1024 nt
	global_load_dwordx2 v[58:59], v[0:1], off offset:3072 nt
	global_load_dwordx2 v[60:61], v[0:1], off offset:1536 nt
	global_load_dwordx2 v[62:63], v[0:1], off offset:3584 nt
	v_addc_co_u32_e32 v37, vcc, 0, v1, vcc
	s_mul_hi_i32 s4, s3, 0x6000
	s_mulk_i32 s3, 0x6000
	global_load_dwordx4 v[16:19], v[4:5], off offset:-3072 nt
	global_load_dwordx4 v[20:23], v[4:5], off offset:-2048 nt
	global_load_dwordx4 v[24:27], v[4:5], off offset:-1024 nt
	global_load_dwordx4 v[28:31], v[4:5], off nt
	global_load_dwordx2 v[64:65], v[36:37], off nt
	global_load_dwordx2 v[66:67], v[36:37], off offset:2048 nt
	global_load_dwordx2 v[68:69], v[36:37], off offset:512 nt
	global_load_dwordx2 v[70:71], v[36:37], off offset:2560 nt
	global_load_dwordx2 v[72:73], v[36:37], off offset:1024 nt
	global_load_dwordx2 v[74:75], v[36:37], off offset:3072 nt
	global_load_dwordx2 v[76:77], v[36:37], off offset:1536 nt
	global_load_dwordx2 v[78:79], v[36:37], off offset:3584 nt
	s_add_u32 s3, s54, s3
	s_addc_u32 s5, s55, s4
	s_add_u32 s4, s3, 0x45000
	s_addc_u32 s5, s5, 0
	global_load_dwordx4 v[36:39], v10, s[4:5]
	global_load_dwordx4 v[40:43], v11, s[4:5]
	global_load_dwordx4 v[44:47], v12, s[4:5]
	global_load_dwordx4 v[48:51], v13, s[4:5]
	s_add_i32 s0, s0, s6
	v_lshl_add_u64 v[0:1], v[0:1], 0, s[8:9]
	s_cmp_lt_i32 s0, 0x10000
	s_waitcnt vmcnt(23)
	v_lshlrev_b32_e32 v80, 16, v8
	v_and_b32_e32 v81, 0xffff0000, v8
	v_lshlrev_b32_e32 v8, 16, v9
	v_and_b32_e32 v9, 0xffff0000, v9
	s_waitcnt vmcnt(21)
	v_lshlrev_b32_e32 v84, 16, v52
	v_and_b32_e32 v85, 0xffff0000, v52
	v_lshlrev_b32_e32 v82, 16, v6
	v_and_b32_e32 v83, 0xffff0000, v6
	v_lshlrev_b32_e32 v6, 16, v7
	v_and_b32_e32 v7, 0xffff0000, v7
	s_waitcnt vmcnt(20)
	v_lshlrev_b32_e32 v86, 16, v54
	v_and_b32_e32 v87, 0xffff0000, v54
	v_lshlrev_b32_e32 v52, 16, v53
	v_and_b32_e32 v53, 0xffff0000, v53
	s_waitcnt vmcnt(19)
	v_lshlrev_b32_e32 v88, 16, v56
	v_and_b32_e32 v89, 0xffff0000, v56
	v_lshlrev_b32_e32 v56, 16, v57
	v_and_b32_e32 v57, 0xffff0000, v57
	s_waitcnt vmcnt(17)
	v_lshlrev_b32_e32 v92, 16, v60
	v_and_b32_e32 v93, 0xffff0000, v60
	v_lshlrev_b32_e32 v60, 16, v61
	v_and_b32_e32 v61, 0xffff0000, v61
	v_pk_add_f32 v[80:81], v[80:81], 0 op_sel_hi:[1,0]
	v_pk_add_f32 v[8:9], v[8:9], 0 op_sel_hi:[1,0]
	v_pk_add_f32 v[84:85], v[84:85], 0 op_sel_hi:[1,0]
	v_lshlrev_b32_e32 v54, 16, v55
	v_and_b32_e32 v55, 0xffff0000, v55
	v_lshlrev_b32_e32 v90, 16, v58
	v_and_b32_e32 v91, 0xffff0000, v58
	v_lshlrev_b32_e32 v58, 16, v59
	v_and_b32_e32 v59, 0xffff0000, v59
	s_waitcnt vmcnt(16)
	v_lshlrev_b32_e32 v94, 16, v62
	v_and_b32_e32 v95, 0xffff0000, v62
	v_lshlrev_b32_e32 v62, 16, v63
	v_and_b32_e32 v63, 0xffff0000, v63
	v_pk_add_f32 v[52:53], v[52:53], 0 op_sel_hi:[1,0]
	v_pk_add_f32 v[88:89], v[88:89], 0 op_sel_hi:[1,0]
	v_pk_add_f32 v[56:57], v[56:57], 0 op_sel_hi:[1,0]
	v_pk_add_f32 v[92:93], v[92:93], 0 op_sel_hi:[1,0]
	v_pk_add_f32 v[60:61], v[60:61], 0 op_sel_hi:[1,0]
	v_pk_add_f32 v[80:81], v[80:81], v[82:83]
	s_waitcnt vmcnt(11)
	v_lshlrev_b32_e32 v82, 16, v64
	v_and_b32_e32 v83, 0xffff0000, v64
	s_waitcnt vmcnt(10)
	v_lshlrev_b32_e32 v96, 16, v66
	v_and_b32_e32 v97, 0xffff0000, v66
	v_pk_add_f32 v[6:7], v[8:9], v[6:7]
	v_lshlrev_b32_e32 v8, 16, v65
	v_and_b32_e32 v9, 0xffff0000, v65
	v_lshlrev_b32_e32 v64, 16, v67
	v_and_b32_e32 v65, 0xffff0000, v67
	v_pk_add_f32 v[66:67], v[84:85], v[86:87]
	s_waitcnt vmcnt(9)
	v_lshlrev_b32_e32 v84, 16, v68
	v_and_b32_e32 v85, 0xffff0000, v68
	s_waitcnt vmcnt(8)
	v_lshlrev_b32_e32 v86, 16, v70
	v_and_b32_e32 v87, 0xffff0000, v70
	v_pk_add_f32 v[52:53], v[52:53], v[54:55]
	v_lshlrev_b32_e32 v54, 16, v69
	v_and_b32_e32 v55, 0xffff0000, v69
	v_lshlrev_b32_e32 v68, 16, v71
	v_and_b32_e32 v69, 0xffff0000, v71
	v_pk_add_f32 v[70:71], v[88:89], v[90:91]
	s_waitcnt vmcnt(7)
	v_lshlrev_b32_e32 v88, 16, v72
	v_and_b32_e32 v89, 0xffff0000, v72
	s_waitcnt vmcnt(6)
; __device__ __forceinline__ void phase_final(const Frame& F, const Params& P) {
;     ...
;             v[j] += *(const f32x4*)(g5 + col) * s;
;             ss += v[j][0] * v[j][0] + v[j][1] * v[j][1] + v[j][2] * v[j][2] + v[j][3] * v[j][3];
;         }
;         ss = wave_sum(ss);
;         const float rstd = rsqrtf(ss * (1.f / 1024.f) + EPS);
; #pragma unroll
;         for (int j = 0; j < 4; ++j) {
;             const int col = F.lane * 4 + 256 * j;
;             const f32x4 gg = *(const f32x4*)(P.g_final + col);
;             f32x4 o;
; #pragma unroll
;             for (int i = 0; i < 4; ++i) o[i] = v[j][i] * rstd * gg[i];
;             *(f32x4*)(xr + col) = o;
;         }
	v_lshlrev_b32_e32 v90, 16, v74
	v_and_b32_e32 v91, 0xffff0000, v74
	v_pk_add_f32 v[56:57], v[56:57], v[58:59]
	v_lshlrev_b32_e32 v58, 16, v73
	v_and_b32_e32 v59, 0xffff0000, v73
	v_lshlrev_b32_e32 v72, 16, v75
	v_and_b32_e32 v73, 0xffff0000, v75
	v_pk_add_f32 v[74:75], v[92:93], v[94:95]
	s_waitcnt vmcnt(5)
	v_lshlrev_b32_e32 v92, 16, v76
	v_and_b32_e32 v93, 0xffff0000, v76
	s_waitcnt vmcnt(4)
	v_lshlrev_b32_e32 v94, 16, v78
	v_and_b32_e32 v95, 0xffff0000, v78
	v_pk_add_f32 v[60:61], v[60:61], v[62:63]
	v_lshlrev_b32_e32 v62, 16, v77
	v_and_b32_e32 v63, 0xffff0000, v77
	v_lshlrev_b32_e32 v76, 16, v79
	v_and_b32_e32 v77, 0xffff0000, v79
	v_pk_add_f32 v[78:79], v[80:81], v[82:83]
	v_pk_add_f32 v[6:7], v[6:7], v[8:9]
	v_pk_add_f32 v[8:9], v[66:67], v[84:85]
	v_pk_add_f32 v[52:53], v[52:53], v[54:55]
	v_pk_add_f32 v[54:55], v[70:71], v[88:89]
	v_pk_add_f32 v[60:61], v[60:61], v[62:63]
	v_pk_add_f32 v[62:63], v[78:79], v[96:97]
	v_pk_add_f32 v[8:9], v[8:9], v[86:87]
	v_pk_add_f32 v[56:57], v[56:57], v[58:59]
	v_pk_add_f32 v[58:59], v[74:75], v[92:93]
	v_pk_add_f32 v[54:55], v[54:55], v[90:91]
	s_waitcnt vmcnt(3)
	v_pk_fma_f32 v[16:17], v[36:37], v[62:63], v[16:17]
	s_waitcnt vmcnt(2)
	v_pk_fma_f32 v[20:21], v[40:41], v[8:9], v[20:21]
	v_pk_add_f32 v[6:7], v[6:7], v[64:65]
	v_pk_add_f32 v[52:53], v[52:53], v[68:69]
	v_pk_add_f32 v[58:59], v[58:59], v[94:95]
	s_waitcnt vmcnt(1)
	v_pk_fma_f32 v[24:25], v[44:45], v[54:55], v[24:25]
	v_mul_f32_e32 v8, v17, v17
	v_mul_f32_e32 v9, v21, v21
	v_pk_add_f32 v[56:57], v[56:57], v[72:73]
	v_pk_add_f32 v[60:61], v[60:61], v[76:77]
	v_pk_fma_f32 v[6:7], v[38:39], v[6:7], v[18:19]
	v_pk_fma_f32 v[18:19], v[42:43], v[52:53], v[22:23]
	s_waitcnt vmcnt(0)
	v_pk_fma_f32 v[28:29], v[48:49], v[58:59], v[28:29]
	v_mul_f32_e32 v15, v25, v25
	v_fmac_f32_e32 v8, v16, v16
	v_fmac_f32_e32 v9, v20, v20
	v_pk_fma_f32 v[22:23], v[46:47], v[56:57], v[26:27]
	v_pk_fma_f32 v[26:27], v[50:51], v[60:61], v[30:31]
	v_mul_f32_e32 v30, v29, v29
	v_fmac_f32_e32 v15, v24, v24
	v_fmac_f32_e32 v8, v6, v6
	v_fmac_f32_e32 v9, v18, v18
	v_fmac_f32_e32 v30, v28, v28
	v_fmac_f32_e32 v15, v22, v22
	v_fmac_f32_e32 v8, v7, v7
	v_fmac_f32_e32 v9, v19, v19
	v_fmac_f32_e32 v30, v26, v26
	v_fmac_f32_e32 v15, v23, v23
	v_add_f32_e32 v8, v8, v9
	v_fmac_f32_e32 v30, v27, v27
	v_add_f32_e32 v8, v8, v15
	v_add_f32_e32 v8, v8, v30
	s_nop 1
	v_add_f32_dpp v8, v8, v8 quad_perm:[1,0,3,2] row_mask:0xf bank_mask:0xf bound_ctrl:1
	s_nop 1
	v_add_f32_dpp v8, v8, v8 quad_perm:[2,3,0,1] row_mask:0xf bank_mask:0xf bound_ctrl:1
	s_nop 1
	v_add_f32_dpp v8, v8, v8 row_half_mirror row_mask:0xf bank_mask:0xf bound_ctrl:1
	s_nop 1
	v_add_f32_dpp v8, v8, v8 row_mirror row_mask:0xf bank_mask:0xf bound_ctrl:1
	v_mov_b32_e32 v9, v8
	s_nop 1
	v_permlane16_swap_b32_e32 v8, v9
	v_add_f32_e32 v8, v8, v9
	v_mov_b32_e32 v9, v8
	s_nop 1
	v_permlane32_swap_b32_e32 v8, v9
	v_add_f32_e32 v8, v8, v9
	v_fmamk_f32 v8, v8, 0x3a800000, v14
	v_mul_f32_e32 v9, 0x4b800000, v8
	v_cmp_gt_f32_e32 vcc, s2, v8
	s_nop 1
	v_cndmask_b32_e32 v8, v8, v9, vcc
	v_rsq_f32_e32 v8, v8
	s_nop 0
	v_mul_f32_e32 v9, 0x45800000, v8
	v_cndmask_b32_e32 v30, v8, v9, vcc
	v_pk_mul_f32 v[16:17], v[16:17], v[30:31] op_sel_hi:[1,0]
	v_pk_mul_f32 v[6:7], v[6:7], v[30:31] op_sel_hi:[1,0]
	s_nop 0
	v_pk_mul_f32 v[8:9], v[100:101], v[6:7]
	v_pk_mul_f32 v[6:7], v[98:99], v[16:17]
	global_store_dwordx4 v[4:5], v[6:9], off offset:-3072
	v_pk_mul_f32 v[16:17], v[18:19], v[30:31] op_sel_hi:[1,0]
	v_pk_mul_f32 v[18:19], v[20:21], v[30:31] op_sel_hi:[1,0]
	s_nop 0
	v_pk_mul_f32 v[34:35], v[104:105], v[16:17]
	v_pk_mul_f32 v[32:33], v[102:103], v[18:19]
	global_store_dwordx4 v[4:5], v[32:35], off offset:-2048
	v_pk_mul_f32 v[16:17], v[22:23], v[30:31] op_sel_hi:[1,0]
	v_pk_mul_f32 v[18:19], v[24:25], v[30:31] op_sel_hi:[1,0]
	s_nop 0
	v_pk_mul_f32 v[46:47], v[108:109], v[16:17]
	v_pk_mul_f32 v[44:45], v[106:107], v[18:19]
	global_store_dwordx4 v[4:5], v[44:47], off offset:-1024
	v_pk_mul_f32 v[16:17], v[26:27], v[30:31] op_sel_hi:[1,0]
	v_pk_mul_f32 v[18:19], v[28:29], v[30:31] op_sel_hi:[1,0]
	s_nop 0
	v_pk_mul_f32 v[42:43], v[112:113], v[16:17]
	v_pk_mul_f32 v[40:41], v[110:111], v[18:19]
	global_store_dwordx4 v[4:5], v[40:43], off
	v_lshl_add_u64 v[4:5], v[4:5], 0, s[10:11]
	s_cbranch_scc1 .LBB0_1932
